# P1 column-max reduction de-serialized; uv4 work-queue index prefetched, slot via ds ops
# speedup vs baseline: 1.0057x; 1.0057x over previous
.LBB0_94:
	s_add_i32 s89, s82, s3
	s_ashr_i32 s10, s89, 31
	s_lshr_b32 s10, s10, 27
	s_add_i32 s10, s89, s10
	s_ashr_i32 s90, s10, 5
	s_andn2_b32 s10, s10, 31
	s_sub_i32 s88, s89, s10
	s_lshl_b32 s87, s90, 8
	s_cmp_eq_u32 s90, s12
	s_cbranch_scc1 .LBB0_151
	s_or_b32 s10, s87, 16
	s_cmpk_gt_i32 s89, 0x2ff
	s_cselect_b32 s10, s10, s87
	s_ashr_i32 s11, s10, 31
	v_mov_b32_e32 v3, v2
	v_lshl_add_u64 v[4:5], s[10:11], 2, v[146:147]
	s_mov_b64 s[98:99], 0xe040
	v_mad_i64_i32 v[200:201], s[100:101], v148, s80, v[4:5]
	global_load_dword v202, v[200:201], off
	v_lshl_add_u64 v[200:201], v[200:201], 0, s[98:99]
	global_load_dword v203, v[200:201], off
	v_lshl_add_u64 v[200:201], v[200:201], 0, s[98:99]
	global_load_dword v204, v[200:201], off
	v_lshl_add_u64 v[200:201], v[200:201], 0, s[98:99]
	global_load_dword v205, v[200:201], off
	v_lshl_add_u64 v[200:201], v[200:201], 0, s[98:99]
	global_load_dword v206, v[200:201], off
	v_lshl_add_u64 v[200:201], v[200:201], 0, s[98:99]
	global_load_dword v207, v[200:201], off
	v_lshl_add_u64 v[200:201], v[200:201], 0, s[98:99]
	global_load_dword v208, v[200:201], off
	v_lshl_add_u64 v[200:201], v[200:201], 0, s[98:99]
	global_load_dword v209, v[200:201], off
	v_lshl_add_u64 v[200:201], v[200:201], 0, s[98:99]
	global_load_dword v210, v[200:201], off
	v_lshl_add_u64 v[200:201], v[200:201], 0, s[98:99]
	global_load_dword v211, v[200:201], off
	v_lshl_add_u64 v[200:201], v[200:201], 0, s[98:99]
	global_load_dword v212, v[200:201], off
	v_lshl_add_u64 v[200:201], v[200:201], 0, s[98:99]
	global_load_dword v213, v[200:201], off
	v_lshl_add_u64 v[200:201], v[200:201], 0, s[98:99]
	global_load_dword v214, v[200:201], off
	v_lshl_add_u64 v[200:201], v[200:201], 0, s[98:99]
	global_load_dword v215, v[200:201], off
	v_lshl_add_u64 v[200:201], v[200:201], 0, s[98:99]
	global_load_dword v216, v[200:201], off
	v_lshl_add_u64 v[200:201], v[200:201], 0, s[98:99]
	global_load_dword v217, v[200:201], off
	v_lshl_add_u64 v[200:201], v[200:201], 0, s[98:99]
	global_load_dword v218, v[200:201], off
	v_lshl_add_u64 v[200:201], v[200:201], 0, s[98:99]
	global_load_dword v219, v[200:201], off
	v_lshl_add_u64 v[200:201], v[200:201], 0, s[98:99]
	global_load_dword v220, v[200:201], off
	v_lshl_add_u64 v[200:201], v[200:201], 0, s[98:99]
	global_load_dword v221, v[200:201], off
	v_lshl_add_u64 v[200:201], v[200:201], 0, s[98:99]
	global_load_dword v222, v[200:201], off
	v_lshl_add_u64 v[200:201], v[200:201], 0, s[98:99]
	global_load_dword v223, v[200:201], off
	v_lshl_add_u64 v[200:201], v[200:201], 0, s[98:99]
	global_load_dword v224, v[200:201], off
	v_lshl_add_u64 v[200:201], v[200:201], 0, s[98:99]
	global_load_dword v225, v[200:201], off
	v_lshl_add_u64 v[200:201], v[200:201], 0, s[98:99]
	global_load_dword v226, v[200:201], off
	v_lshl_add_u64 v[200:201], v[200:201], 0, s[98:99]
	global_load_dword v227, v[200:201], off
	v_lshl_add_u64 v[200:201], v[200:201], 0, s[98:99]
	global_load_dword v228, v[200:201], off
	v_lshl_add_u64 v[200:201], v[200:201], 0, s[98:99]
	global_load_dword v229, v[200:201], off
	v_lshl_add_u64 v[200:201], v[200:201], 0, s[98:99]
	global_load_dword v230, v[200:201], off
	v_lshl_add_u64 v[200:201], v[200:201], 0, s[98:99]
	global_load_dword v231, v[200:201], off
	v_lshl_add_u64 v[200:201], v[200:201], 0, s[98:99]
	global_load_dword v232, v[200:201], off
	v_lshl_add_u64 v[200:201], v[200:201], 0, s[98:99]
	global_load_dword v233, v[200:201], off
	s_waitcnt vmcnt(0)
	v_max3_f32 v70, v202, v203, v204
	v_max3_f32 v70, v70, v205, v206
	v_max3_f32 v70, v70, v207, v208
	v_max3_f32 v70, v70, v209, v210
	v_max3_f32 v70, v70, v211, v212
	v_max3_f32 v70, v70, v213, v214
	v_max3_f32 v70, v70, v215, v216
	v_max3_f32 v70, v70, v217, v218
	v_max3_f32 v70, v70, v219, v220
	v_max3_f32 v70, v70, v221, v222
	v_max3_f32 v70, v70, v223, v224
	v_max3_f32 v70, v70, v225, v226
	v_max3_f32 v70, v70, v227, v228
	v_max3_f32 v70, v70, v229, v230
	v_max3_f32 v70, v70, v231, v232
	v_max3_f32 v70, v70, v233, 0
	ds_write_b32 v154, v70 offset:36864
	s_waitcnt lgkmcnt(0)
	s_barrier
	s_and_saveexec_b64 s[10:11], s[6:7]
	s_cbranch_execz .LBB0_150
	ds_read2st64_b32 v[4:5], v154 offset0:144 offset1:148
	s_cmp_lg_u32 s88, 0
	s_waitcnt lgkmcnt(0)
	v_max3_f32 v3, v4, v5, s83
	v_mul_f32_e32 v3, 0x3c010204, v3
	v_div_scale_f32 v4, s[12:13], v3, v3, 1.0
	v_rcp_f32_e32 v5, v4
	v_div_scale_f32 v70, vcc, 1.0, v3, 1.0
	v_fma_f32 v71, -v4, v5, 1.0
	v_fmac_f32_e32 v5, v71, v5
	v_mul_f32_e32 v71, v70, v5
	v_fma_f32 v72, -v4, v71, v70
	v_fmac_f32_e32 v71, v72, v5
	v_fma_f32 v4, -v4, v71, v70
	v_div_fmas_f32 v4, v4, v5, v71
	v_div_fixup_f32 v4, v4, v3, 1.0
	ds_write_b32 v154, v4 offset:38912
	s_cbranch_scc1 .LBB0_150
	v_add_u32_e32 v4, s87, v149
	v_ashrrev_i32_e32 v5, 31, v4
	v_lshl_add_u64 v[4:5], v[4:5], 2, s[8:9]
	global_store_dword v[4:5], v3, off

.LBB0_155:
	s_or_b32 s10, s10, s3
	s_ashr_i32 s14, s10, 31
	s_lshr_b32 s14, s14, 27
	s_add_i32 s14, s10, s14
	s_ashr_i32 s90, s14, 5
	s_andn2_b32 s14, s14, 31
	s_sub_i32 s89, s10, s14
	s_lshl_b32 s10, s90, 8
	s_cmp_eq_u32 s90, s11
	s_cbranch_scc1 .LBB0_212
	s_ashr_i32 s11, s10, 31
	v_mov_b32_e32 v3, v2
	v_lshl_add_u64 v[4:5], s[10:11], 2, v[148:149]
	s_mov_b64 s[98:99], 0x4000
	v_lshlrev_b32_e32 v200, 14, v146
	v_mov_b32_e32 v201, 0
	v_lshl_add_u64 v[200:201], v[4:5], 0, v[200:201]
	global_load_dword v202, v[200:201], off
	v_lshl_add_u64 v[200:201], v[200:201], 0, s[98:99]
	global_load_dword v203, v[200:201], off
	v_lshl_add_u64 v[200:201], v[200:201], 0, s[98:99]
	global_load_dword v204, v[200:201], off
	v_lshl_add_u64 v[200:201], v[200:201], 0, s[98:99]
	global_load_dword v205, v[200:201], off
	v_lshl_add_u64 v[200:201], v[200:201], 0, s[98:99]
	global_load_dword v206, v[200:201], off
	v_lshl_add_u64 v[200:201], v[200:201], 0, s[98:99]
	global_load_dword v207, v[200:201], off
	v_lshl_add_u64 v[200:201], v[200:201], 0, s[98:99]
	global_load_dword v208, v[200:201], off
	v_lshl_add_u64 v[200:201], v[200:201], 0, s[98:99]
	global_load_dword v209, v[200:201], off
	v_lshl_add_u64 v[200:201], v[200:201], 0, s[98:99]
	global_load_dword v210, v[200:201], off
	v_lshl_add_u64 v[200:201], v[200:201], 0, s[98:99]
	global_load_dword v211, v[200:201], off
	v_lshl_add_u64 v[200:201], v[200:201], 0, s[98:99]
	global_load_dword v212, v[200:201], off
	v_lshl_add_u64 v[200:201], v[200:201], 0, s[98:99]
	global_load_dword v213, v[200:201], off
	v_lshl_add_u64 v[200:201], v[200:201], 0, s[98:99]
	global_load_dword v214, v[200:201], off
	v_lshl_add_u64 v[200:201], v[200:201], 0, s[98:99]
	global_load_dword v215, v[200:201], off
	v_lshl_add_u64 v[200:201], v[200:201], 0, s[98:99]
	global_load_dword v216, v[200:201], off
	v_lshl_add_u64 v[200:201], v[200:201], 0, s[98:99]
	global_load_dword v217, v[200:201], off
	v_lshl_add_u64 v[200:201], v[200:201], 0, s[98:99]
	global_load_dword v218, v[200:201], off
	v_lshl_add_u64 v[200:201], v[200:201], 0, s[98:99]
	global_load_dword v219, v[200:201], off
	v_lshl_add_u64 v[200:201], v[200:201], 0, s[98:99]
	global_load_dword v220, v[200:201], off
	v_lshl_add_u64 v[200:201], v[200:201], 0, s[98:99]
	global_load_dword v221, v[200:201], off
	v_lshl_add_u64 v[200:201], v[200:201], 0, s[98:99]
	global_load_dword v222, v[200:201], off
	v_lshl_add_u64 v[200:201], v[200:201], 0, s[98:99]
	global_load_dword v223, v[200:201], off
	v_lshl_add_u64 v[200:201], v[200:201], 0, s[98:99]
	global_load_dword v224, v[200:201], off
	v_lshl_add_u64 v[200:201], v[200:201], 0, s[98:99]
	global_load_dword v225, v[200:201], off
	v_lshl_add_u64 v[200:201], v[200:201], 0, s[98:99]
	global_load_dword v226, v[200:201], off
	v_lshl_add_u64 v[200:201], v[200:201], 0, s[98:99]
	global_load_dword v227, v[200:201], off
	v_lshl_add_u64 v[200:201], v[200:201], 0, s[98:99]
	global_load_dword v228, v[200:201], off
	v_lshl_add_u64 v[200:201], v[200:201], 0, s[98:99]
	global_load_dword v229, v[200:201], off
	v_lshl_add_u64 v[200:201], v[200:201], 0, s[98:99]
	global_load_dword v230, v[200:201], off
	v_lshl_add_u64 v[200:201], v[200:201], 0, s[98:99]
	global_load_dword v231, v[200:201], off
	v_lshl_add_u64 v[200:201], v[200:201], 0, s[98:99]
	global_load_dword v232, v[200:201], off
	v_lshl_add_u64 v[200:201], v[200:201], 0, s[98:99]
	global_load_dword v233, v[200:201], off
	s_waitcnt vmcnt(0)
	v_max3_f32 v70, v202, v203, v204
	v_max3_f32 v70, v70, v205, v206
	v_max3_f32 v70, v70, v207, v208
	v_max3_f32 v70, v70, v209, v210
	v_max3_f32 v70, v70, v211, v212
	v_max3_f32 v70, v70, v213, v214
	v_max3_f32 v70, v70, v215, v216
	v_max3_f32 v70, v70, v217, v218
	v_max3_f32 v70, v70, v219, v220
	v_max3_f32 v70, v70, v221, v222
	v_max3_f32 v70, v70, v223, v224
	v_max3_f32 v70, v70, v225, v226
	v_max3_f32 v70, v70, v227, v228
	v_max3_f32 v70, v70, v229, v230
	v_max3_f32 v70, v70, v231, v232
	v_max3_f32 v70, v70, v233, 0
	ds_write_b32 v183, v70 offset:36864
	s_waitcnt lgkmcnt(0)
	s_barrier
	s_and_saveexec_b64 s[14:15], s[6:7]
	s_cbranch_execz .LBB0_211
	ds_read2st64_b32 v[4:5], v183 offset0:144 offset1:148
	s_cmp_lg_u32 s89, 0
	s_waitcnt lgkmcnt(0)
	v_max3_f32 v3, v4, v5, s86
	v_mul_f32_e32 v3, 0x3c010204, v3
	v_div_scale_f32 v4, s[16:17], v3, v3, 1.0
	v_rcp_f32_e32 v5, v4
	v_div_scale_f32 v70, vcc, 1.0, v3, 1.0
	v_fma_f32 v71, -v4, v5, 1.0
	v_fmac_f32_e32 v5, v71, v5
	v_mul_f32_e32 v71, v70, v5
	v_fma_f32 v72, -v4, v71, v70
	v_fmac_f32_e32 v71, v72, v5
	v_fma_f32 v4, -v4, v71, v70
	v_div_fmas_f32 v4, v4, v5, v71
	v_div_fixup_f32 v4, v4, v3, 1.0
	ds_write_b32 v183, v4 offset:38912
	s_cbranch_scc1 .LBB0_211
	v_add_u32_e32 v4, s10, v147
	v_ashrrev_i32_e32 v5, 31, v4
	v_lshl_add_u64 v[4:5], v[4:5], 2, s[8:9]
	global_store_dword v[4:5], v3, off

.LBB0_1386:
	s_mov_b64 s[6:7], s[0:1]
	s_barrier
	s_mov_b64 s[8:9], s[0:1]
	s_load_dwordx2 s[6:7], s[6:7], 0x90
	s_load_dwordx2 s[16:17], s[8:9], 0x78
	s_mov_b64 s[8:9], s[0:1]
	s_load_dwordx2 s[18:19], s[8:9], 0x80
	s_mov_b64 s[8:9], s[0:1]
	s_load_dwordx2 s[8:9], s[8:9], 0x90
	s_waitcnt lgkmcnt(0)
	s_add_u32 s20, s6, 0x8000
	s_addc_u32 s21, s7, 0
	s_mov_b64 s[6:7], s[0:1]
	s_mov_b64 s[14:15], src_shared_base
	s_add_u32 s3, s8, 0xa300000
	s_addc_u32 s14, s9, 0
	s_load_dwordx2 s[6:7], s[6:7], 0x90
	s_mov_b64 s[8:9], s[0:1]
	s_load_dwordx2 s[8:9], s[8:9], 0x90
	s_mov_b64 s[10:11], s[0:1]
	s_load_dwordx2 s[10:11], s[10:11], 0x90
	s_waitcnt lgkmcnt(0)
	s_add_u32 s28, s6, 0xe300000
	s_addc_u32 s29, s7, 0
	s_add_u32 s30, s8, 0x12300000
	v_mov_b32_e32 v3, v0
	s_addc_u32 s31, s9, 0
	v_mbcnt_hi_u32_b32 v1, -1, v1
	v_and_b32_e32 v2, 63, v3
	s_add_u32 s34, s10, 0x16300000
	v_ashrrev_i32_e32 v72, 6, v3
	v_cmp_eq_u32_e64 s[6:7], 0, v3
	v_lshlrev_b32_e32 v4, 2, v2
	v_and_b32_e32 v3, 64, v1
	s_addc_u32 s35, s11, 0
	v_mov_b32_e32 v67, 0
	v_cmp_eq_u32_e64 s[8:9], 0, v2
	s_mov_b64 s[22:23], 0
	s_movk_i32 s36, 0x1000
	s_movk_i32 s37, 0x3fff
	v_lshlrev_b32_e32 v66, 2, v4
	s_movk_i32 s38, 0x2000
	s_movk_i32 s39, 0x3000
	s_waitcnt vmcnt(0)
	v_add_u32_e32 v154, 64, v3
	v_xor_b32_e32 v157, 1, v1
	v_xor_b32_e32 v158, 2, v1
	v_xor_b32_e32 v159, 4, v1
	v_xor_b32_e32 v160, 8, v1
	v_xor_b32_e32 v156, 16, v1
	v_xor_b32_e32 v155, 32, v1
	s_mov_b32 s40, 0xf800000
	v_mov_b32_e32 v73, 0x260
	s_mov_b32 s41, 0x8080808
	v_lshlrev_b32_e32 v68, 2, v2
	s_mov_b32 s42, 0x400000
	s_mov_b32 s43, 0x800000
	s_mov_b32 s52, 0xc00000
	s_mov_b32 s53, 0x1000000
	v_mov_b32_e32 v74, 0x41700000
	s_and_saveexec_b64 s[98:99], s[6:7]
	s_cbranch_execz .Luv4_pro_done
	v_mov_b32_e32 v250, 1
	global_atomic_add v250, v67, v250, s[20:21] sc0
	s_waitcnt vmcnt(0)
.Luv4_pro_done:
	s_or_b64 exec, exec, s[98:99]
	s_branch .LBB0_1389

.LBB0_1389:
	s_barrier
	s_and_saveexec_b64 s[10:11], s[6:7]
	s_cbranch_execz .Luv4_slot_written
	v_mov_b32_e32 v2, 0
	ds_write_b32 v2, v250
.Luv4_slot_written:
	s_or_b64 exec, exec, s[10:11]
	v_mov_b32_e32 v2, 0
	s_waitcnt lgkmcnt(0)
	s_barrier
	ds_read_b32 v2, v2
	s_mov_b64 s[10:11], -1
	s_waitcnt lgkmcnt(0)
	v_cmp_gt_u32_e32 vcc, s36, v2
	s_and_saveexec_b64 s[24:25], vcc
	s_cbranch_execz .LBB0_1388
	v_lshl_add_u32 v2, v2, 3, v72
	v_add_u32_e32 v3, 0xffffc000, v2
	v_cmp_lt_i32_e64 s[10:11], s37, v2
	v_mov_b32_e32 v4, s18
	s_nop 0
	v_cndmask_b32_e64 v70, v2, v3, s[10:11]
	v_mov_b32_e32 v2, s17
	v_mov_b32_e32 v3, s19
	v_cndmask_b32_e64 v3, v2, v3, s[10:11]
	v_mov_b32_e32 v2, s16
	v_ashrrev_i32_e32 v71, 31, v70
	v_cndmask_b32_e64 v2, v2, v4, s[10:11]
	v_lshlrev_b64 v[4:5], 14, v[70:71]
	v_lshl_add_u64 v[2:3], v[2:3], 0, v[4:5]
	v_lshl_add_u64 v[2:3], v[2:3], 0, v[66:67]
	s_and_saveexec_b64 s[98:99], s[6:7]
	s_cbranch_execz .Luv4_next_issued
	v_mov_b32_e32 v250, 1
	global_atomic_add v250, v67, v250, s[20:21] sc0
.Luv4_next_issued:
	s_or_b64 exec, exec, s[98:99]
	v_add_co_u32_e32 v34, vcc, s38, v2
	global_load_dwordx4 v[46:49], v[2:3], off
	global_load_dwordx4 v[30:33], v[2:3], off offset:1024
	global_load_dwordx4 v[26:29], v[2:3], off offset:2048
	global_load_dwordx4 v[18:21], v[2:3], off offset:3072
	v_addc_co_u32_e32 v35, vcc, 0, v3, vcc
	global_load_dwordx4 v[22:25], v[34:35], off offset:-4096
	v_add_co_u32_e32 v4, vcc, s36, v2
	s_waitcnt vmcnt(4)
	v_mul_f32_e32 v42, v47, v47
	v_addc_co_u32_e32 v5, vcc, 0, v3, vcc
	global_load_dwordx4 v[10:13], v[4:5], off offset:1024
	v_add_co_u32_e32 v36, vcc, s39, v2
	v_mul_f32_e32 v43, v49, v49
	s_nop 0
	v_addc_co_u32_e32 v37, vcc, 0, v3, vcc
	global_load_dwordx4 v[62:65], v[4:5], off offset:2048
	global_load_dwordx4 v[50:53], v[4:5], off offset:3072
	global_load_dwordx4 v[38:41], v[34:35], off
	global_load_dwordx4 v[14:17], v[34:35], off offset:1024
	global_load_dwordx4 v[6:9], v[34:35], off offset:2048
	s_nop 0
	global_load_dwordx4 v[2:5], v[36:37], off offset:3072
	v_max_f32_e64 v44, |v47|, |v47|
	v_max_f32_e64 v45, |v46|, |v46|
	v_max_f32_e64 v54, |v49|, |v49|
	v_max_f32_e64 v55, |v48|, |v48|
	s_waitcnt vmcnt(10)
	v_mul_f32_e32 v56, v31, v31
	v_mul_f32_e32 v57, v33, v33
	s_waitcnt vmcnt(9)
	v_mul_f32_e32 v69, v27, v27
	v_mul_f32_e32 v75, v29, v29
	v_fmac_f32_e32 v42, v46, v46
	v_fmac_f32_e32 v43, v48, v48
	v_max_f32_e32 v44, v45, v44
	v_max_f32_e32 v45, v55, v54
	v_fmac_f32_e32 v56, v30, v30
	v_fmac_f32_e32 v57, v32, v32
	v_max_f32_e64 v58, |v31|, |v31|
	v_max_f32_e64 v59, |v30|, |v30|
	v_max_f32_e64 v76, |v27|, |v27|
	v_max_f32_e64 v77, |v26|, |v26|
	s_waitcnt vmcnt(8)
	v_mul_f32_e32 v80, v19, v19
	v_mul_f32_e32 v81, v21, v21
	v_fmac_f32_e32 v69, v26, v26
	v_fmac_f32_e32 v75, v28, v28
	v_add_f32_e32 v42, v42, v43
	v_max3_f32 v43, v44, 0, v45
	v_add_f32_e32 v44, v56, v57
	v_max_f32_e32 v54, v59, v58
	v_max_f32_e32 v58, v77, v76
	v_fmac_f32_e32 v80, v18, v18
	v_fmac_f32_e32 v81, v20, v20
	s_waitcnt vmcnt(7)
	v_mul_f32_e32 v76, v23, v23
	v_mul_f32_e32 v77, v25, v25
	v_add_f32_e32 v45, v69, v75
	v_add_f32_e32 v42, v42, v44
	v_max_f32_e64 v60, |v33|, |v33|
	v_max_f32_e64 v61, |v32|, |v32|
	v_add_f32_e32 v56, v80, v81
	v_fmac_f32_e32 v76, v22, v22
	v_fmac_f32_e32 v77, v24, v24
	v_add_f32_e32 v42, v42, v45
	v_max_f32_e64 v78, |v29|, |v29|
	v_max_f32_e64 v79, |v28|, |v28|
	v_max_f32_e32 v55, v61, v60
	v_add_f32_e32 v42, v42, v56
	v_add_f32_e32 v44, v76, v77
	v_max_f32_e64 v82, |v19|, |v19|
	v_max_f32_e64 v83, |v18|, |v18|
	v_max_f32_e64 v84, |v21|, |v21|
	v_max_f32_e64 v85, |v20|, |v20|
	v_max_f32_e32 v59, v79, v78
	v_max3_f32 v43, v43, v54, v55
	v_add_f32_e32 v42, v42, v44
	v_max_f32_e64 v44, |v23|, |v23|
	v_max_f32_e64 v45, |v22|, |v22|
	v_max_f32_e32 v60, v83, v82
	v_max_f32_e32 v61, v85, v84
	v_max3_f32 v43, v43, v58, v59
	v_max_f32_e32 v44, v45, v44
	v_max_f32_e64 v45, |v25|, |v25|
	v_max_f32_e64 v54, |v24|, |v24|
	v_max3_f32 v43, v43, v60, v61
	v_max_f32_e32 v45, v54, v45
	v_max3_f32 v43, v43, v44, v45
	global_load_dwordx4 v[58:61], v[34:35], off offset:3072
	global_load_dwordx4 v[54:57], v[36:37], off
	v_cmp_lt_i32_e32 vcc, v157, v154
	s_waitcnt vmcnt(8)
	v_mul_f32_e32 v44, v11, v11
	v_mul_f32_e32 v34, v13, v13
	v_fmac_f32_e32 v44, v10, v10
	v_fmac_f32_e32 v34, v12, v12
	v_add_f32_e32 v34, v44, v34
	v_add_f32_e32 v34, v42, v34
	v_max_f32_e64 v35, |v11|, |v11|
	v_max_f32_e64 v42, |v10|, |v10|
	v_max_f32_e32 v35, v42, v35
	v_max_f32_e64 v42, |v13|, |v13|
	v_max_f32_e64 v44, |v12|, |v12|
	v_max_f32_e32 v42, v44, v42
	v_max3_f32 v35, v43, v35, v42
	s_waitcnt vmcnt(7)
	v_mul_f32_e32 v42, v63, v63
	v_mul_f32_e32 v43, v65, v65
	v_fmac_f32_e32 v42, v62, v62
	v_fmac_f32_e32 v43, v64, v64
	v_add_f32_e32 v42, v42, v43
	v_add_f32_e32 v34, v34, v42
	v_max_f32_e64 v42, |v63|, |v63|
	v_max_f32_e64 v43, |v62|, |v62|
	v_max_f32_e32 v42, v43, v42
	v_max_f32_e64 v43, |v65|, |v65|
	v_max_f32_e64 v44, |v64|, |v64|
	v_max_f32_e32 v43, v44, v43
	v_max3_f32 v69, v35, v42, v43
	global_load_dwordx4 v[42:45], v[36:37], off offset:1024
	s_waitcnt vmcnt(7)
	v_mul_f32_e32 v35, v51, v51
	v_mul_f32_e32 v75, v53, v53
	v_fmac_f32_e32 v35, v50, v50
	v_fmac_f32_e32 v75, v52, v52
	v_add_f32_e32 v35, v35, v75
	v_add_f32_e32 v75, v34, v35
	v_max_f32_e64 v34, |v51|, |v51|
	v_max_f32_e64 v35, |v50|, |v50|
	v_max_f32_e32 v76, v35, v34
	v_max_f32_e64 v34, |v53|, |v53|
	v_max_f32_e64 v35, |v52|, |v52|
	v_max_f32_e32 v77, v35, v34
	global_load_dwordx4 v[34:37], v[36:37], off offset:2048
	v_max3_f32 v69, v69, v76, v77
	s_waitcnt vmcnt(7)
	v_mul_f32_e32 v76, v39, v39
	v_mul_f32_e32 v77, v41, v41
	v_fmac_f32_e32 v76, v38, v38
	v_fmac_f32_e32 v77, v40, v40
	v_add_f32_e32 v76, v76, v77
	v_add_f32_e32 v75, v75, v76
	v_max_f32_e64 v76, |v39|, |v39|
	v_max_f32_e64 v77, |v38|, |v38|
	v_max_f32_e32 v76, v77, v76
	v_max_f32_e64 v77, |v41|, |v41|
	v_max_f32_e64 v78, |v40|, |v40|
	v_max_f32_e32 v77, v78, v77
	v_max3_f32 v69, v69, v76, v77
	s_waitcnt vmcnt(6)
	v_mul_f32_e32 v76, v15, v15
	v_mul_f32_e32 v77, v17, v17
	v_fmac_f32_e32 v76, v14, v14
	v_fmac_f32_e32 v77, v16, v16
	v_add_f32_e32 v76, v76, v77
	v_add_f32_e32 v75, v75, v76
	v_max_f32_e64 v76, |v15|, |v15|
	v_max_f32_e64 v77, |v14|, |v14|
	v_max_f32_e32 v76, v77, v76
	v_max_f32_e64 v77, |v17|, |v17|
	v_max_f32_e64 v78, |v16|, |v16|
	v_max_f32_e32 v77, v78, v77
	v_max3_f32 v69, v69, v76, v77
	s_waitcnt vmcnt(5)
	v_mul_f32_e32 v76, v7, v7
	v_mul_f32_e32 v77, v9, v9
	v_fmac_f32_e32 v76, v6, v6
	v_fmac_f32_e32 v77, v8, v8
	v_add_f32_e32 v76, v76, v77
	v_add_f32_e32 v75, v75, v76
	v_max_f32_e64 v76, |v7|, |v7|
	v_max_f32_e64 v77, |v6|, |v6|
	v_max_f32_e32 v76, v77, v76
	v_max_f32_e64 v77, |v9|, |v9|
	v_max_f32_e64 v78, |v8|, |v8|
	v_max_f32_e32 v77, v78, v77
	v_max3_f32 v69, v69, v76, v77
	s_waitcnt vmcnt(3)
	v_mul_f32_e32 v76, v59, v59
	v_mul_f32_e32 v77, v61, v61
	v_fmac_f32_e32 v76, v58, v58
	v_fmac_f32_e32 v77, v60, v60
	v_add_f32_e32 v76, v76, v77
	v_add_f32_e32 v75, v75, v76
	v_max_f32_e64 v76, |v59|, |v59|
	v_max_f32_e64 v77, |v58|, |v58|
	v_max_f32_e32 v76, v77, v76
	v_max_f32_e64 v77, |v61|, |v61|
	v_max_f32_e64 v78, |v60|, |v60|
	v_max_f32_e32 v77, v78, v77
	v_max3_f32 v69, v69, v76, v77
	s_waitcnt vmcnt(2)
	v_mul_f32_e32 v76, v55, v55
	v_mul_f32_e32 v77, v57, v57
	v_fmac_f32_e32 v76, v54, v54
	v_fmac_f32_e32 v77, v56, v56
	v_add_f32_e32 v76, v76, v77
	v_add_f32_e32 v75, v75, v76
	v_max_f32_e64 v76, |v55|, |v55|
	v_max_f32_e64 v77, |v54|, |v54|
	v_max_f32_e32 v76, v77, v76
	v_max_f32_e64 v77, |v57|, |v57|
	v_max_f32_e64 v78, |v56|, |v56|
	v_max_f32_e32 v77, v78, v77
	v_max3_f32 v69, v69, v76, v77
	s_waitcnt vmcnt(1)
	v_mul_f32_e32 v76, v43, v43
	v_mul_f32_e32 v77, v45, v45
	v_fmac_f32_e32 v76, v42, v42
	v_fmac_f32_e32 v77, v44, v44
	v_add_f32_e32 v76, v76, v77
	v_add_f32_e32 v75, v75, v76
	v_max_f32_e64 v76, |v43|, |v43|
	v_max_f32_e64 v77, |v42|, |v42|
	v_max_f32_e32 v76, v77, v76
	v_max_f32_e64 v77, |v45|, |v45|
	v_max_f32_e64 v78, |v44|, |v44|
	v_max_f32_e32 v77, v78, v77
	v_max3_f32 v69, v69, v76, v77
	s_waitcnt vmcnt(0)
	v_mul_f32_e32 v76, v35, v35
	v_mul_f32_e32 v77, v37, v37
	v_fmac_f32_e32 v76, v34, v34
	v_fmac_f32_e32 v77, v36, v36
	v_add_f32_e32 v76, v76, v77
	v_add_f32_e32 v75, v75, v76
	v_max_f32_e64 v76, |v35|, |v35|
	v_max_f32_e64 v77, |v34|, |v34|
	v_max_f32_e32 v76, v77, v76
	v_max_f32_e64 v77, |v37|, |v37|
	v_max_f32_e64 v78, |v36|, |v36|
	v_max_f32_e32 v77, v78, v77
	v_max3_f32 v69, v69, v76, v77
	v_mul_f32_e32 v76, v3, v3
	v_mul_f32_e32 v77, v5, v5
	v_fmac_f32_e32 v76, v2, v2
	v_fmac_f32_e32 v77, v4, v4
	v_add_f32_e32 v76, v76, v77
	v_add_f32_e32 v75, v75, v76
	v_max_f32_e64 v76, |v3|, |v3|
	v_max_f32_e64 v77, |v2|, |v2|
	v_max_f32_e32 v76, v77, v76
	v_max_f32_e64 v77, |v5|, |v5|
	v_max_f32_e64 v80, |v4|, |v4|
	v_cndmask_b32_e32 v78, v1, v157, vcc
	v_max_f32_e32 v77, v80, v77
	v_lshlrev_b32_e32 v78, 2, v78
	v_max3_f32 v69, v69, v76, v77
	ds_bpermute_b32 v79, v78, v75
	ds_bpermute_b32 v76, v78, v69
	v_cmp_lt_i32_e32 vcc, v158, v154
	s_waitcnt lgkmcnt(1)
	v_add_f32_e32 v75, v75, v79
	v_cndmask_b32_e32 v77, v1, v158, vcc
	v_lshlrev_b32_e32 v77, 2, v77
	s_waitcnt lgkmcnt(0)
	v_max_f32_e32 v76, v76, v76
	ds_bpermute_b32 v78, v77, v75
	v_max_f32_e32 v69, v69, v76
	ds_bpermute_b32 v76, v77, v69
	v_cmp_lt_i32_e32 vcc, v159, v154
	s_waitcnt lgkmcnt(1)
	v_add_f32_e32 v75, v75, v78
	v_cndmask_b32_e32 v77, v1, v159, vcc
	v_lshlrev_b32_e32 v77, 2, v77
	ds_bpermute_b32 v78, v77, v75
	s_waitcnt lgkmcnt(1)
	v_max_f32_e32 v76, v76, v76
	v_max_f32_e32 v69, v69, v76
	ds_bpermute_b32 v76, v77, v69
	v_cmp_lt_i32_e32 vcc, v160, v154
	s_waitcnt lgkmcnt(1)
	v_add_f32_e32 v75, v75, v78
	s_waitcnt lgkmcnt(0)
	v_max_f32_e32 v76, v76, v76
	v_cndmask_b32_e32 v77, v1, v160, vcc
	v_lshlrev_b32_e32 v77, 2, v77
	ds_bpermute_b32 v78, v77, v75
	v_max_f32_e32 v69, v69, v76
	ds_bpermute_b32 v76, v77, v69
	v_cmp_lt_i32_e32 vcc, v156, v154
	s_waitcnt lgkmcnt(1)
	v_add_f32_e32 v75, v75, v78
	v_cndmask_b32_e32 v77, v1, v156, vcc
	v_lshlrev_b32_e32 v77, 2, v77
	ds_bpermute_b32 v78, v77, v75
	s_waitcnt lgkmcnt(1)
	v_max_f32_e32 v76, v76, v76
	v_max_f32_e32 v69, v69, v76
	v_cmp_lt_i32_e32 vcc, v155, v154
	ds_bpermute_b32 v76, v77, v69
	s_waitcnt lgkmcnt(1)
	v_add_f32_e32 v75, v75, v78
	v_cndmask_b32_e32 v77, v1, v155, vcc
	v_lshlrev_b32_e32 v77, 2, v77
	ds_bpermute_b32 v78, v77, v75
	s_waitcnt lgkmcnt(1)
	v_max_f32_e32 v76, v76, v76
	v_max_f32_e32 v69, v69, v76
	ds_bpermute_b32 v76, v77, v69
	s_waitcnt lgkmcnt(1)
	v_add_f32_e32 v75, v75, v78
	v_mul_f32_e32 v75, 0x39800000, v75
	v_mul_f32_e32 v77, 0x4f800000, v75
	v_cmp_gt_f32_e32 vcc, s40, v75
	s_waitcnt lgkmcnt(0)
	v_max_f32_e32 v76, v76, v76
	v_max_f32_e32 v69, v69, v76
	v_cndmask_b32_e32 v75, v75, v77, vcc
	v_sqrt_f32_e32 v77, v75
	v_mul_f32_e32 v69, 0x3e088889, v69
	v_add_u32_e32 v76, -1, v77
	v_fma_f32 v78, -v76, v77, v75
	v_cmp_ge_f32_e64 s[12:13], 0, v78
	v_add_u32_e32 v78, 1, v77
	s_nop 0
	v_cndmask_b32_e64 v76, v77, v76, s[12:13]
	v_fma_f32 v77, -v78, v77, v75
	v_cmp_lt_f32_e64 s[12:13], 0, v77
	s_nop 1
	v_cndmask_b32_e64 v76, v76, v78, s[12:13]
	v_mul_f32_e32 v77, 0x37800000, v76
	v_cndmask_b32_e32 v76, v76, v77, vcc
	v_cmp_class_f32_e32 vcc, v75, v73
	s_nop 1
	v_cndmask_b32_e32 v75, v76, v75, vcc
	v_mul_f32_e32 v75, 0x3eab9f56, v75
	v_min_f32_e32 v69, v75, v69
	v_max_f32_e32 v75, 0xda24260, v69
	v_div_scale_f32 v69, s[12:13], v75, v75, 1.0
	v_rcp_f32_e32 v76, v69
	s_nop 0
	v_fma_f32 v77, -v69, v76, 1.0
	v_fmac_f32_e32 v76, v77, v76
	v_div_scale_f32 v77, vcc, 1.0, v75, 1.0
	v_mul_f32_e32 v78, v77, v76
	v_fma_f32 v79, -v69, v78, v77
	v_fmac_f32_e32 v78, v79, v76
	v_fma_f32 v69, -v69, v78, v77
	v_div_fmas_f32 v69, v69, v76, v78
	v_div_fixup_f32 v69, v69, v75, 1.0
	v_mul_f32_e32 v19, v19, v69
	v_mul_f32_e32 v18, v18, v69
	v_floor_f32_e32 v19, v19
	v_mul_f32_e32 v20, v20, v69
	v_floor_f32_e32 v18, v18
	v_add_f32_e32 v19, 0x41000000, v19
	v_floor_f32_e32 v20, v20
	v_add_f32_e32 v18, 0x41000000, v18
	v_med3_f32 v19, v19, 0, v74
	v_add_f32_e32 v20, 0x41000000, v20
	v_med3_f32 v18, v18, 0, v74
	v_cvt_i32_f32_e32 v19, v19
	v_med3_f32 v20, v20, 0, v74
	v_cvt_i32_f32_e32 v18, v18
	v_cvt_i32_f32_sdwa v20, v20 dst_sel:WORD_1 dst_unused:UNUSED_PAD src0_sel:DWORD
	v_lshlrev_b32_e32 v19, 8, v19
	v_mul_f32_e32 v11, v11, v69
	v_mul_f32_e32 v10, v10, v69
	v_or3_b32 v18, v19, v18, v20
	v_mul_f32_e32 v19, v21, v69
	v_mul_f32_e32 v21, v23, v69
	v_floor_f32_e32 v19, v19
	v_mul_f32_e32 v20, v22, v69
	v_floor_f32_e32 v21, v21
	v_mul_f32_e32 v22, v24, v69
	v_add_f32_e32 v19, 0x41000000, v19
	v_floor_f32_e32 v20, v20
	v_add_f32_e32 v21, 0x41000000, v21
	v_floor_f32_e32 v22, v22
	v_mul_f32_e32 v23, v25, v69
	v_floor_f32_e32 v11, v11
	v_mul_f32_e32 v12, v12, v69
	v_med3_f32 v19, v19, 0, v74
	v_add_f32_e32 v20, 0x41000000, v20
	v_med3_f32 v21, v21, 0, v74
	v_add_f32_e32 v22, 0x41000000, v22
	v_floor_f32_e32 v23, v23
	v_floor_f32_e32 v10, v10
	v_add_f32_e32 v11, 0x41000000, v11
	v_floor_f32_e32 v12, v12
	v_mul_f32_e32 v15, v15, v69
	v_cvt_i32_f32_sdwa v19, v19 dst_sel:BYTE_3 dst_unused:UNUSED_PAD src0_sel:DWORD
	v_med3_f32 v20, v20, 0, v74
	v_cvt_i32_f32_e32 v21, v21
	v_med3_f32 v22, v22, 0, v74
	v_add_f32_e32 v23, 0x41000000, v23
	v_add_f32_e32 v10, 0x41000000, v10
	v_med3_f32 v11, v11, 0, v74
	v_add_f32_e32 v12, 0x41000000, v12
	v_mul_f32_e32 v14, v14, v69
	v_floor_f32_e32 v15, v15
	v_mul_f32_e32 v16, v16, v69
	v_cvt_i32_f32_e32 v20, v20
	v_cvt_i32_f32_sdwa v22, v22 dst_sel:WORD_1 dst_unused:UNUSED_PAD src0_sel:DWORD
	v_med3_f32 v23, v23, 0, v74
	v_med3_f32 v10, v10, 0, v74
	v_cvt_i32_f32_e32 v11, v11
	v_med3_f32 v12, v12, 0, v74
	v_floor_f32_e32 v14, v14
	v_add_f32_e32 v15, 0x41000000, v15
	v_floor_f32_e32 v16, v16
	v_cvt_i32_f32_sdwa v23, v23 dst_sel:BYTE_3 dst_unused:UNUSED_PAD src0_sel:DWORD
	v_cvt_i32_f32_e32 v10, v10
	v_cvt_i32_f32_sdwa v12, v12 dst_sel:WORD_1 dst_unused:UNUSED_PAD src0_sel:DWORD
	v_add_f32_e32 v14, 0x41000000, v14
	v_med3_f32 v15, v15, 0, v74
	v_add_f32_e32 v16, 0x41000000, v16
	v_med3_f32 v14, v14, 0, v74
	v_cvt_i32_f32_e32 v15, v15
	v_med3_f32 v16, v16, 0, v74
	v_bitop3_b32 v18, v18, s41, v19 bitop3:0x36
	v_lshlrev_b32_e32 v19, 8, v21
	v_cvt_i32_f32_e32 v14, v14
	v_cvt_i32_f32_sdwa v16, v16 dst_sel:WORD_1 dst_unused:UNUSED_PAD src0_sel:DWORD
	v_or3_b32 v19, v19, v20, v22
	v_lshlrev_b32_e32 v11, 8, v11
	v_or_b32_e32 v20, v19, v23
	v_bitop3_b32 v19, v19, s41, v23 bitop3:0x36
	v_or3_b32 v10, v11, v10, v12
	v_mul_f32_e32 v11, v13, v69
	v_mul_f32_e32 v13, v63, v69
	v_cndmask_b32_e64 v19, v19, v20, s[10:11]
	v_floor_f32_e32 v11, v11
	v_mul_f32_e32 v12, v62, v69
	v_floor_f32_e32 v13, v13
	v_mul_f32_e32 v20, v64, v69
	v_lshlrev_b32_e32 v15, 8, v15
	v_add_f32_e32 v11, 0x41000000, v11
	v_floor_f32_e32 v12, v12
	v_add_f32_e32 v13, 0x41000000, v13
	v_floor_f32_e32 v20, v20
	v_or3_b32 v14, v15, v14, v16
	v_mul_f32_e32 v15, v17, v69
	v_mul_f32_e32 v7, v7, v69
	v_med3_f32 v11, v11, 0, v74
	v_add_f32_e32 v12, 0x41000000, v12
	v_med3_f32 v13, v13, 0, v74
	v_add_f32_e32 v20, 0x41000000, v20
	v_floor_f32_e32 v15, v15
	v_mul_f32_e32 v6, v6, v69
	v_floor_f32_e32 v7, v7
	v_mul_f32_e32 v8, v8, v69
	v_cvt_i32_f32_sdwa v11, v11 dst_sel:BYTE_3 dst_unused:UNUSED_PAD src0_sel:DWORD
	v_med3_f32 v12, v12, 0, v74
	v_cvt_i32_f32_e32 v13, v13
	v_med3_f32 v20, v20, 0, v74
	v_add_f32_e32 v15, 0x41000000, v15
	v_floor_f32_e32 v6, v6
	v_add_f32_e32 v7, 0x41000000, v7
	v_floor_f32_e32 v8, v8
	v_cvt_i32_f32_e32 v12, v12
	v_cvt_i32_f32_sdwa v20, v20 dst_sel:WORD_1 dst_unused:UNUSED_PAD src0_sel:DWORD
	v_med3_f32 v15, v15, 0, v74
	v_add_f32_e32 v6, 0x41000000, v6
	v_med3_f32 v7, v7, 0, v74
	v_add_f32_e32 v8, 0x41000000, v8
	v_cvt_i32_f32_sdwa v15, v15 dst_sel:BYTE_3 dst_unused:UNUSED_PAD src0_sel:DWORD
	v_med3_f32 v6, v6, 0, v74
	v_cvt_i32_f32_e32 v7, v7
	v_med3_f32 v8, v8, 0, v74
	v_cvt_i32_f32_e32 v6, v6
	v_cvt_i32_f32_sdwa v8, v8 dst_sel:WORD_1 dst_unused:UNUSED_PAD src0_sel:DWORD
	v_mul_f32_e32 v21, v65, v69
	v_bitop3_b32 v10, v10, s41, v11 bitop3:0x36
	v_lshlrev_b32_e32 v11, 8, v13
	v_floor_f32_e32 v21, v21
	v_or3_b32 v11, v11, v12, v20
	v_mul_f32_e32 v20, v51, v69
	v_mul_f32_e32 v9, v9, v69
	v_add_f32_e32 v21, 0x41000000, v21
	v_mul_f32_e32 v13, v50, v69
	v_floor_f32_e32 v20, v20
	v_mul_f32_e32 v22, v52, v69
	v_floor_f32_e32 v9, v9
	v_bitop3_b32 v14, v14, s41, v15 bitop3:0x36
	v_lshlrev_b32_e32 v7, 8, v7
	v_mul_f32_e32 v15, v59, v69
	v_med3_f32 v21, v21, 0, v74
	v_floor_f32_e32 v13, v13
	v_add_f32_e32 v20, 0x41000000, v20
	v_floor_f32_e32 v22, v22
	v_add_f32_e32 v9, 0x41000000, v9
	v_or3_b32 v6, v7, v6, v8
	v_mul_f32_e32 v8, v58, v69
	v_floor_f32_e32 v15, v15
	v_mul_f32_e32 v16, v60, v69
	v_cvt_i32_f32_sdwa v21, v21 dst_sel:BYTE_3 dst_unused:UNUSED_PAD src0_sel:DWORD
	v_add_f32_e32 v13, 0x41000000, v13
	v_med3_f32 v20, v20, 0, v74
	v_add_f32_e32 v22, 0x41000000, v22
	v_med3_f32 v9, v9, 0, v74
	v_floor_f32_e32 v8, v8
	v_add_f32_e32 v15, 0x41000000, v15
	v_floor_f32_e32 v16, v16
	v_med3_f32 v13, v13, 0, v74
	v_cvt_i32_f32_e32 v20, v20
	v_med3_f32 v22, v22, 0, v74
	v_cvt_i32_f32_sdwa v9, v9 dst_sel:BYTE_3 dst_unused:UNUSED_PAD src0_sel:DWORD
	v_add_f32_e32 v8, 0x41000000, v8
	v_med3_f32 v15, v15, 0, v74
	v_add_f32_e32 v16, 0x41000000, v16
	v_cvt_i32_f32_e32 v13, v13
	v_cvt_i32_f32_sdwa v22, v22 dst_sel:WORD_1 dst_unused:UNUSED_PAD src0_sel:DWORD
	v_med3_f32 v8, v8, 0, v74
	v_cvt_i32_f32_e32 v15, v15
	v_med3_f32 v16, v16, 0, v74
	v_cvt_i32_f32_e32 v8, v8
	v_cvt_i32_f32_sdwa v16, v16 dst_sel:WORD_1 dst_unused:UNUSED_PAD src0_sel:DWORD
	v_or_b32_e32 v12, v11, v21
	v_bitop3_b32 v11, v11, s41, v21 bitop3:0x36
	v_cndmask_b32_e64 v11, v11, v12, s[10:11]
	v_lshlrev_b32_e32 v12, 8, v20
	v_or_b32_e32 v7, v6, v9
	v_bitop3_b32 v6, v6, s41, v9 bitop3:0x36
	v_or3_b32 v12, v12, v13, v22
	v_mul_f32_e32 v13, v53, v69
	v_mul_f32_e32 v21, v39, v69
	v_cndmask_b32_e64 v6, v6, v7, s[10:11]
	v_lshlrev_b32_e32 v7, 8, v15
	v_floor_f32_e32 v13, v13
	v_mul_f32_e32 v20, v38, v69
	v_floor_f32_e32 v21, v21
	v_mul_f32_e32 v22, v40, v69
	v_or3_b32 v7, v7, v8, v16
	v_mul_f32_e32 v8, v61, v69
	v_mul_f32_e32 v15, v55, v69
	v_add_f32_e32 v13, 0x41000000, v13
	v_floor_f32_e32 v20, v20
	v_add_f32_e32 v21, 0x41000000, v21
	v_floor_f32_e32 v22, v22
	v_mul_f32_e32 v23, v41, v69
	v_floor_f32_e32 v8, v8
	v_mul_f32_e32 v9, v54, v69
	v_floor_f32_e32 v15, v15
	v_mul_f32_e32 v16, v56, v69
	v_med3_f32 v13, v13, 0, v74
	v_add_f32_e32 v20, 0x41000000, v20
	v_med3_f32 v21, v21, 0, v74
	v_add_f32_e32 v22, 0x41000000, v22
	v_floor_f32_e32 v23, v23
	v_add_f32_e32 v8, 0x41000000, v8
	v_floor_f32_e32 v9, v9
	v_add_f32_e32 v15, 0x41000000, v15
	v_floor_f32_e32 v16, v16
	v_cvt_i32_f32_sdwa v13, v13 dst_sel:BYTE_3 dst_unused:UNUSED_PAD src0_sel:DWORD
	v_med3_f32 v20, v20, 0, v74
	v_cvt_i32_f32_e32 v21, v21
	v_med3_f32 v22, v22, 0, v74
	v_add_f32_e32 v23, 0x41000000, v23
	v_med3_f32 v8, v8, 0, v74
	v_add_f32_e32 v9, 0x41000000, v9
	v_med3_f32 v15, v15, 0, v74
	v_add_f32_e32 v16, 0x41000000, v16
	v_cvt_i32_f32_e32 v20, v20
	v_cvt_i32_f32_sdwa v22, v22 dst_sel:WORD_1 dst_unused:UNUSED_PAD src0_sel:DWORD
	v_med3_f32 v23, v23, 0, v74
	v_cvt_i32_f32_sdwa v8, v8 dst_sel:BYTE_3 dst_unused:UNUSED_PAD src0_sel:DWORD
	v_med3_f32 v9, v9, 0, v74
	v_cvt_i32_f32_e32 v15, v15
	v_med3_f32 v16, v16, 0, v74
	v_cvt_i32_f32_sdwa v23, v23 dst_sel:BYTE_3 dst_unused:UNUSED_PAD src0_sel:DWORD
	v_cvt_i32_f32_e32 v9, v9
	v_cvt_i32_f32_sdwa v16, v16 dst_sel:WORD_1 dst_unused:UNUSED_PAD src0_sel:DWORD
	v_bitop3_b32 v12, v12, s41, v13 bitop3:0x36
	v_lshlrev_b32_e32 v13, 8, v21
	v_or3_b32 v13, v13, v20, v22
	v_mul_f32_e32 v17, v57, v69
	v_bitop3_b32 v7, v7, s41, v8 bitop3:0x36
	v_lshlrev_b32_e32 v8, 8, v15
	v_or_b32_e32 v20, v13, v23
	v_bitop3_b32 v13, v13, s41, v23 bitop3:0x36
	v_floor_f32_e32 v17, v17
	v_or3_b32 v8, v8, v9, v16
	v_mul_f32_e32 v16, v43, v69
	v_cndmask_b32_e64 v13, v13, v20, s[10:11]
	v_add_f32_e32 v17, 0x41000000, v17
	v_mul_f32_e32 v15, v42, v69
	v_floor_f32_e32 v16, v16
	v_mul_f32_e32 v20, v44, v69
	v_med3_f32 v17, v17, 0, v74
	v_floor_f32_e32 v15, v15
	v_add_f32_e32 v16, 0x41000000, v16
	v_floor_f32_e32 v20, v20
	v_cvt_i32_f32_sdwa v17, v17 dst_sel:BYTE_3 dst_unused:UNUSED_PAD src0_sel:DWORD
	v_add_f32_e32 v15, 0x41000000, v15
	v_med3_f32 v16, v16, 0, v74
	v_add_f32_e32 v20, 0x41000000, v20
	v_med3_f32 v15, v15, 0, v74
	v_cvt_i32_f32_e32 v16, v16
	v_med3_f32 v20, v20, 0, v74
	v_cvt_i32_f32_e32 v15, v15
	v_cvt_i32_f32_sdwa v20, v20 dst_sel:WORD_1 dst_unused:UNUSED_PAD src0_sel:DWORD
	v_mul_f32_e32 v31, v31, v69
	v_mul_f32_e32 v30, v30, v69
	v_floor_f32_e32 v31, v31
	v_mul_f32_e32 v32, v32, v69
	v_or_b32_e32 v9, v8, v17
	v_bitop3_b32 v8, v8, s41, v17 bitop3:0x36
	v_floor_f32_e32 v30, v30
	v_add_f32_e32 v31, 0x41000000, v31
	v_floor_f32_e32 v32, v32
	v_cndmask_b32_e64 v8, v8, v9, s[10:11]
	v_lshlrev_b32_e32 v9, 8, v16
	v_add_f32_e32 v30, 0x41000000, v30
	v_med3_f32 v31, v31, 0, v74
	v_add_f32_e32 v32, 0x41000000, v32
	v_or3_b32 v9, v9, v15, v20
	v_mul_f32_e32 v15, v45, v69
	v_mul_f32_e32 v17, v35, v69
	v_med3_f32 v30, v30, 0, v74
	v_cvt_i32_f32_e32 v31, v31
	v_med3_f32 v32, v32, 0, v74
	v_floor_f32_e32 v15, v15
	v_mul_f32_e32 v16, v34, v69
	v_floor_f32_e32 v17, v17
	v_mul_f32_e32 v20, v36, v69
	v_mul_f32_e32 v3, v3, v69
	v_cvt_i32_f32_e32 v30, v30
	v_cvt_i32_f32_sdwa v32, v32 dst_sel:WORD_1 dst_unused:UNUSED_PAD src0_sel:DWORD
	v_add_f32_e32 v15, 0x41000000, v15
	v_floor_f32_e32 v16, v16
	v_add_f32_e32 v17, 0x41000000, v17
	v_floor_f32_e32 v20, v20
	v_mul_f32_e32 v21, v37, v69
	v_mul_f32_e32 v2, v2, v69
	v_floor_f32_e32 v3, v3
	v_mul_f32_e32 v4, v4, v69
	v_mul_f32_e32 v47, v47, v69
	v_med3_f32 v15, v15, 0, v74
	v_add_f32_e32 v16, 0x41000000, v16
	v_med3_f32 v17, v17, 0, v74
	v_add_f32_e32 v20, 0x41000000, v20
	v_floor_f32_e32 v21, v21
	v_floor_f32_e32 v2, v2
	v_add_f32_e32 v3, 0x41000000, v3
	v_floor_f32_e32 v4, v4
	v_mul_f32_e32 v5, v5, v69
	v_mul_f32_e32 v46, v46, v69
	v_floor_f32_e32 v47, v47
	v_mul_f32_e32 v48, v48, v69
	v_cvt_i32_f32_sdwa v15, v15 dst_sel:BYTE_3 dst_unused:UNUSED_PAD src0_sel:DWORD
	v_med3_f32 v16, v16, 0, v74
	v_cvt_i32_f32_e32 v17, v17
	v_med3_f32 v20, v20, 0, v74
	v_add_f32_e32 v21, 0x41000000, v21
	v_add_f32_e32 v2, 0x41000000, v2
	v_med3_f32 v3, v3, 0, v74
	v_add_f32_e32 v4, 0x41000000, v4
	v_floor_f32_e32 v5, v5
	v_floor_f32_e32 v46, v46
	v_add_f32_e32 v47, 0x41000000, v47
	v_floor_f32_e32 v48, v48
	v_mul_f32_e32 v49, v49, v69
	v_lshlrev_b32_e32 v31, 8, v31
	v_mul_f32_e32 v27, v27, v69
	v_cvt_i32_f32_e32 v16, v16
	v_cvt_i32_f32_sdwa v20, v20 dst_sel:WORD_1 dst_unused:UNUSED_PAD src0_sel:DWORD
	v_med3_f32 v21, v21, 0, v74
	v_med3_f32 v2, v2, 0, v74
	v_cvt_i32_f32_e32 v3, v3
	v_med3_f32 v4, v4, 0, v74
	v_add_f32_e32 v5, 0x41000000, v5
	v_add_f32_e32 v46, 0x41000000, v46
	v_med3_f32 v47, v47, 0, v74
	v_add_f32_e32 v48, 0x41000000, v48
	v_floor_f32_e32 v49, v49
	v_or3_b32 v30, v31, v30, v32
	v_mul_f32_e32 v31, v33, v69
	v_mul_f32_e32 v26, v26, v69
	v_floor_f32_e32 v27, v27
	v_mul_f32_e32 v28, v28, v69
	v_cvt_i32_f32_sdwa v21, v21 dst_sel:BYTE_3 dst_unused:UNUSED_PAD src0_sel:DWORD
	v_cvt_i32_f32_e32 v2, v2
	v_cvt_i32_f32_sdwa v4, v4 dst_sel:WORD_1 dst_unused:UNUSED_PAD src0_sel:DWORD
	v_med3_f32 v5, v5, 0, v74
	v_med3_f32 v46, v46, 0, v74
	v_cvt_i32_f32_e32 v47, v47
	v_med3_f32 v48, v48, 0, v74
	v_add_f32_e32 v49, 0x41000000, v49
	v_floor_f32_e32 v31, v31
	v_floor_f32_e32 v26, v26
	v_add_f32_e32 v27, 0x41000000, v27
	v_floor_f32_e32 v28, v28
	v_mul_f32_e32 v29, v29, v69
	v_cvt_i32_f32_sdwa v5, v5 dst_sel:BYTE_3 dst_unused:UNUSED_PAD src0_sel:DWORD
	v_cvt_i32_f32_e32 v46, v46
	v_cvt_i32_f32_sdwa v48, v48 dst_sel:WORD_1 dst_unused:UNUSED_PAD src0_sel:DWORD
	v_med3_f32 v49, v49, 0, v74
	v_add_f32_e32 v31, 0x41000000, v31
	v_add_f32_e32 v26, 0x41000000, v26
	v_med3_f32 v27, v27, 0, v74
	v_add_f32_e32 v28, 0x41000000, v28
	v_floor_f32_e32 v29, v29
	v_bitop3_b32 v9, v9, s41, v15 bitop3:0x36
	v_lshlrev_b32_e32 v15, 8, v17
	v_cvt_i32_f32_sdwa v49, v49 dst_sel:BYTE_3 dst_unused:UNUSED_PAD src0_sel:DWORD
	v_med3_f32 v31, v31, 0, v74
	v_med3_f32 v26, v26, 0, v74
	v_cvt_i32_f32_e32 v27, v27
	v_med3_f32 v28, v28, 0, v74
	v_add_f32_e32 v29, 0x41000000, v29
	v_or3_b32 v15, v15, v16, v20
	v_lshlrev_b32_e32 v3, 8, v3
	v_cvt_i32_f32_sdwa v31, v31 dst_sel:BYTE_3 dst_unused:UNUSED_PAD src0_sel:DWORD
	v_cvt_i32_f32_e32 v26, v26
	v_cvt_i32_f32_sdwa v28, v28 dst_sel:WORD_1 dst_unused:UNUSED_PAD src0_sel:DWORD
	v_med3_f32 v29, v29, 0, v74
	v_or_b32_e32 v16, v15, v21
	v_bitop3_b32 v15, v15, s41, v21 bitop3:0x36
	v_or3_b32 v2, v3, v2, v4
	v_lshlrev_b32_e32 v47, 8, v47
	v_cvt_i32_f32_sdwa v29, v29 dst_sel:BYTE_3 dst_unused:UNUSED_PAD src0_sel:DWORD
	v_cndmask_b32_e64 v15, v15, v16, s[10:11]
	v_bitop3_b32 v16, v2, s41, v5 bitop3:0x36
	v_mov_b32_e32 v2, s14
	v_mov_b32_e32 v3, s31
	v_or3_b32 v46, v47, v46, v48
	v_cndmask_b32_e64 v3, v2, v3, s[10:11]
	v_mov_b32_e32 v2, s3
	v_mov_b32_e32 v4, s30
	v_or_b32_e32 v47, v46, v49
	v_bitop3_b32 v46, v46, s41, v49 bitop3:0x36
	v_lshlrev_b32_e32 v27, 8, v27
	v_cndmask_b32_e64 v2, v2, v4, s[10:11]
	v_lshlrev_b64 v[4:5], 8, v[70:71]
	v_cndmask_b32_e64 v46, v46, v47, s[10:11]
	v_bitop3_b32 v30, v30, s41, v31 bitop3:0x36
	v_or3_b32 v26, v27, v26, v28
	v_lshl_add_u64 v[2:3], v[2:3], 0, v[4:5]
	v_mov_b32_e32 v69, v67
	v_or_b32_e32 v27, v26, v29
	v_bitop3_b32 v26, v26, s41, v29 bitop3:0x36
	v_lshl_add_u64 v[2:3], v[2:3], 0, v[68:69]
	v_lshl_or_b32 v4, v30, 4, v46
	v_cndmask_b32_e64 v26, v26, v27, s[10:11]
	global_store_dword v[2:3], v4, off
	v_add_co_u32_e32 v4, vcc, s42, v2
	v_lshl_or_b32 v17, v18, 4, v26
	s_nop 0
	v_addc_co_u32_e32 v5, vcc, 0, v3, vcc
	global_store_dword v[4:5], v17, off
	v_add_co_u32_e32 v4, vcc, s43, v2
	v_lshl_or_b32 v10, v10, 4, v19
	s_nop 0
	v_addc_co_u32_e32 v5, vcc, 0, v3, vcc
	global_store_dword v[4:5], v10, off
	v_add_co_u32_e32 v4, vcc, s52, v2
	v_lshl_or_b32 v10, v12, 4, v11
	s_nop 0
	v_addc_co_u32_e32 v5, vcc, 0, v3, vcc
	global_store_dword v[4:5], v10, off
	v_add_co_u32_e32 v4, vcc, s53, v2
	v_lshl_or_b32 v10, v14, 4, v13
	s_nop 0
	v_addc_co_u32_e32 v5, vcc, 0, v3, vcc
	global_store_dword v[4:5], v10, off
	v_add_co_u32_e32 v4, vcc, 0x1400000, v2
	v_lshl_or_b32 v6, v7, 4, v6
	s_nop 0
	v_addc_co_u32_e32 v5, vcc, 0, v3, vcc
	global_store_dword v[4:5], v6, off
	v_add_co_u32_e32 v4, vcc, 0x1800000, v2
	v_lshl_or_b32 v6, v9, 4, v8
	s_nop 0
	v_addc_co_u32_e32 v5, vcc, 0, v3, vcc
	v_add_co_u32_e32 v2, vcc, 0x1c00000, v2
	global_store_dword v[4:5], v6, off
	v_lshl_or_b32 v4, v16, 4, v15
	v_addc_co_u32_e32 v3, vcc, 0, v3, vcc
	global_store_dword v[2:3], v4, off
	s_and_saveexec_b64 s[12:13], s[8:9]
	s_cbranch_execz .LBB0_1387
	v_mov_b32_e32 v2, s29
	v_mov_b32_e32 v3, s35
	v_cndmask_b32_e64 v3, v2, v3, s[10:11]
	v_mov_b32_e32 v2, s28
	v_mov_b32_e32 v4, s34
	v_cndmask_b32_e64 v2, v2, v4, s[10:11]
	v_lshl_add_u64 v[2:3], v[70:71], 2, v[2:3]
	global_store_dword v[2:3], v75, off
	s_branch .LBB0_1387

	.amdhsa_kernel _Z8mega_fwd6Params
		.amdhsa_group_segment_fixed_size 0
		.amdhsa_private_segment_fixed_size 0
		.amdhsa_kernarg_size 408
		.amdhsa_user_sgpr_count 2
		.amdhsa_user_sgpr_dispatch_ptr 0
		.amdhsa_user_sgpr_queue_ptr 0
		.amdhsa_user_sgpr_kernarg_segment_ptr 1
		.amdhsa_user_sgpr_dispatch_id 0
		.amdhsa_user_sgpr_kernarg_preload_length 0
		.amdhsa_user_sgpr_kernarg_preload_offset 0
		.amdhsa_user_sgpr_private_segment_size 0
		.amdhsa_uses_dynamic_stack 0
		.amdhsa_enable_private_segment 0
		.amdhsa_system_sgpr_workgroup_id_x 1
		.amdhsa_system_sgpr_workgroup_id_y 0
		.amdhsa_system_sgpr_workgroup_id_z 0
		.amdhsa_system_sgpr_workgroup_info 0
		.amdhsa_system_vgpr_workitem_id 0
		.amdhsa_next_free_vgpr 256
		.amdhsa_next_free_sgpr 102
		.amdhsa_accum_offset 256
		.amdhsa_reserve_vcc 1
		.amdhsa_float_round_mode_32 0
		.amdhsa_float_round_mode_16_64 0
		.amdhsa_float_denorm_mode_32 3
		.amdhsa_float_denorm_mode_16_64 3
		.amdhsa_dx10_clamp 1
		.amdhsa_ieee_mode 1
		.amdhsa_fp16_overflow 0
		.amdhsa_tg_split 0
		.amdhsa_exception_fp_ieee_invalid_op 0
		.amdhsa_exception_fp_denorm_src 0
		.amdhsa_exception_fp_ieee_div_zero 0
		.amdhsa_exception_fp_ieee_overflow 0
		.amdhsa_exception_fp_ieee_underflow 0
		.amdhsa_exception_fp_ieee_inexact 0
		.amdhsa_exception_int_div_zero 0
	.end_amdhsa_kernel

amdhsa.kernels:
  - .agpr_count:     0
    .args:
      - .offset:         0
        .size:           152
        .value_kind:     by_value
      - .offset:         152
        .size:           4
        .value_kind:     hidden_block_count_x
      - .offset:         156
        .size:           4
        .value_kind:     hidden_block_count_y
      - .offset:         160
        .size:           4
        .value_kind:     hidden_block_count_z
      - .offset:         164
        .size:           2
        .value_kind:     hidden_group_size_x
      - .offset:         166
        .size:           2
        .value_kind:     hidden_group_size_y
      - .offset:         168
        .size:           2
        .value_kind:     hidden_group_size_z
      - .offset:         170
        .size:           2
        .value_kind:     hidden_remainder_x
      - .offset:         172
        .size:           2
        .value_kind:     hidden_remainder_y
      - .offset:         174
        .size:           2
        .value_kind:     hidden_remainder_z
      - .offset:         192
        .size:           8
        .value_kind:     hidden_global_offset_x
      - .offset:         200
        .size:           8
        .value_kind:     hidden_global_offset_y
      - .offset:         208
        .size:           8
        .value_kind:     hidden_global_offset_z
      - .offset:         216
        .size:           2
        .value_kind:     hidden_grid_dims
      - .offset:         272
        .size:           4
        .value_kind:     hidden_dynamic_lds_size
    .group_segment_fixed_size: 0
    .kernarg_segment_align: 8
    .kernarg_segment_size: 408
    .language:       OpenCL C
    .language_version:
      - 2
      - 0
    .max_flat_workgroup_size: 512
    .name:           _Z8mega_fwd6Params
    .private_segment_fixed_size: 0
    .sgpr_count:     108
    .sgpr_spill_count: 0
    .symbol:         _Z8mega_fwd6Params.kd
    .uniform_work_group_size: 1
    .uses_dynamic_stack: false
    .vgpr_count:     256
    .vgpr_spill_count: 0
    .wavefront_size: 64
